# v33 + SB non-diagonal tile in product form: one reciprocal per 4-key group, w_k = e_k*S_k, range-checked fallback to the original code
# baseline (speedup 1.0000x reference)
; #define LAS __attribute__((address_space(3)))
; __device__ __forceinline__ float fexp2(float x) { return __builtin_amdgcn_exp2f(x); }
; __device__ __forceinline__ float frcp(float x) { return __builtin_amdgcn_rcpf(x); }
; __device__ __forceinline__ float vmul(float a, float b) { float r; asm("v_mul_f32 %0, %1, %2" : "=v"(r) : "v"(a), "v"(b)); return r; }
; template <bool DIAG> __device__ __forceinline__ void sb_tile(const LAS unsigned char* ks, int vpo, const bf16x8 (&qr)[4], f32x16& o0, f32x16& o1, float& carry, int kb, int q, int r32, int hi) {
;     ...
; #pragma unroll
;     for (int d0 = 0; d0 < 4; ++d0) { kf[2 * d0] = *(const LAS bf16x8*)(ks + (2 * d0 + hi) * 1024 + r32 * 16); kf[2 * d0 + 1] = *(const LAS bf16x8*)(ks + (2 * d0 + hi) * 1024 + 512 + r32 * 16); }
;     __builtin_amdgcn_sched_barrier(0);
; #pragma unroll
;     for (int d0 = 0; d0 < 4; ++d0) { z0 = __builtin_amdgcn_mfma_f32_32x32x16_bf16(kf[2 * d0], qr[d0], z0, 0, 0, 0); z1 = __builtin_amdgcn_mfma_f32_32x32x16_bf16(kf[2 * d0 + 1], qr[d0], z1, 0, 0, 0); }
;     v_load(vf, ks + 8192 + vpo);
;     __builtin_amdgcn_sched_barrier(0);
;     f32x16 s0, s1;
; #pragma unroll
;     for (int r = 0; r < 16; ++r) { s0[r] = frcp(1.f + fexp2(z0[r])); s1[r] = frcp(1.f + fexp2(z1[r])); }
;     ...
;     for (int g = 0; g < 4; ++g) {
;         s0[4 * g + 2] = vmul(s0[4 * g + 2], s0[4 * g + 3]); s0[4 * g + 1] = vmul(s0[4 * g + 1], s0[4 * g + 2]); s0[4 * g] = vmul(s0[4 * g], s0[4 * g + 1]);
;         s1[4 * g + 2] = vmul(s1[4 * g + 2], s1[4 * g + 3]); s1[4 * g + 1] = vmul(s1[4 * g + 1], s1[4 * g + 2]); s1[4 * g] = vmul(s1[4 * g], s1[4 * g + 1]);
.LBB0_880:
	s_andn2_b64 vcc, exec, s[14:15]
	s_cbranch_vccnz .LBB0_877
	s_mul_hi_u32 s7, s2, 0xaaaaaaab
	s_add_i32 s14, s95, s80
	s_lshr_b32 s7, s7, 2
	s_max_i32 s16, s14, 0
	s_mul_i32 s7, s7, 0xfffe8000
	v_mad_u64_u32 v[34:35], s[14:15], s16, v234, v[116:117]
	s_add_i32 s7, s33, s7
	v_lshl_add_u64 v[34:35], v[34:35], 0, s[28:29]
	s_add_i32 s17, s7, 0x14000
	s_mov_b32 s14, m0
	s_mov_b32 m0, s17
	s_nop 0
	global_load_lds_dwordx4 v[34:35], off
	s_mov_b32 m0, s14
	s_add_i32 s7, s7, 0x16000
	v_mad_u64_u32 v[34:35], s[14:15], s16, v234, v[118:119]
	v_lshl_add_u64 v[34:35], v[34:35], 0, s[30:31]
	s_mov_b32 s14, m0
	s_mov_b32 m0, s7
	s_nop 0
	global_load_lds_dwordx4 v[34:35], off
	s_mov_b32 m0, s14
	s_add_i32 s7, s97, s6
	s_add_i32 s14, s7, 3
	s_cmp_ge_i32 s14, s83
	s_cselect_b64 s[16:17], -1, 0
	s_or_b64 s[10:11], s[16:17], s[10:11]
	s_and_b64 vcc, exec, s[10:11]
	s_cbranch_vccnz .LBB0_887
	s_mul_hi_i32 s10, s14, 0x2aaaaaab
	s_lshr_b32 s11, s10, 31
	s_add_i32 s10, s10, s11
	s_mul_i32 s10, s10, 6
	s_sub_i32 s10, s14, s10
	s_lshl_b32 s10, s10, 14
	s_add_i32 s14, s10, 0
	v_add_u32_e32 v0, s14, v121
	s_mov_b64 s[10:11], -1
	s_and_b64 vcc, exec, s[12:13]
	v_add3_u32 v126, s14, v123, v122
	v_add_u32_e32 v0, 0x2000, v0
	s_cbranch_vccz .LBB0_884
	ds_read_b128 v[34:37], v126
	ds_read_b128 v[50:53], v126 offset:512
	ds_read_b128 v[82:85], v126 offset:2048
	ds_read_b128 v[86:89], v126 offset:2560
	ds_read_b128 v[90:93], v126 offset:4096
	ds_read_b128 v[94:97], v126 offset:4608
	ds_read_b128 v[98:101], v126 offset:6144
	ds_read_b128 v[102:105], v126 offset:6656
	s_waitcnt lgkmcnt(7)
	v_mfma_f32_32x32x16_bf16 v[34:49], v[34:37], v[78:81], 0
	ds_read_b64_tr_b16 v[110:111], v0 offset:0
	ds_read_b64_tr_b16 v[112:113], v0 offset:512
	ds_read_b64_tr_b16 v[106:107], v0 offset:4096
	ds_read_b64_tr_b16 v[108:109], v0 offset:4608
	s_waitcnt lgkmcnt(6)
	v_mfma_f32_32x32x16_bf16 v[50:65], v[50:53], v[78:81], 0
	s_waitcnt lgkmcnt(5)
	v_mfma_f32_32x32x16_bf16 v[34:49], v[82:85], v[74:77], v[34:49]
	s_waitcnt lgkmcnt(4)
	v_mfma_f32_32x32x16_bf16 v[50:65], v[86:89], v[74:77], v[50:65]
	s_waitcnt lgkmcnt(3)
	v_mfma_f32_32x32x16_bf16 v[34:49], v[90:93], v[70:73], v[34:49]
	s_waitcnt lgkmcnt(2)
	v_mfma_f32_32x32x16_bf16 v[50:65], v[94:97], v[70:73], v[50:65]
	s_waitcnt lgkmcnt(1)
	v_mfma_f32_32x32x16_bf16 v[34:49], v[98:101], v[66:69], v[34:49]
	s_waitcnt lgkmcnt(0)
	v_mfma_f32_32x32x16_bf16 v[50:65], v[102:105], v[66:69], v[50:65]
	ds_read_b64_tr_b16 v[102:103], v0 offset:1024
	ds_read_b64_tr_b16 v[104:105], v0 offset:1536
	ds_read_b64_tr_b16 v[98:99], v0 offset:5120
	ds_read_b64_tr_b16 v[100:101], v0 offset:5632
	ds_read_b64_tr_b16 v[94:95], v0 offset:2048
	ds_read_b64_tr_b16 v[96:97], v0 offset:2560
	ds_read_b64_tr_b16 v[90:91], v0 offset:6144
	ds_read_b64_tr_b16 v[92:93], v0 offset:6656
	ds_read_b64_tr_b16 v[86:87], v0 offset:3072
	ds_read_b64_tr_b16 v[88:89], v0 offset:3584
	ds_read_b64_tr_b16 v[82:83], v0 offset:7168
	ds_read_b64_tr_b16 v[84:85], v0 offset:7680
	s_nop 9
	v_exp_f32_e32 v34, v34
	s_nop 0
	v_exp_f32_e32 v50, v50
	v_exp_f32_e32 v35, v35
	v_exp_f32_e32 v51, v51
	v_exp_f32_e32 v36, v36
	v_exp_f32_e32 v52, v52
	v_exp_f32_e32 v37, v37
	v_exp_f32_e32 v53, v53
	v_exp_f32_e32 v38, v38
	v_exp_f32_e32 v54, v54
	v_exp_f32_e32 v39, v39
	v_exp_f32_e32 v55, v55
	v_exp_f32_e32 v40, v40
	v_exp_f32_e32 v56, v56
	v_exp_f32_e32 v41, v41
	v_exp_f32_e32 v57, v57
	v_exp_f32_e32 v42, v42
	v_exp_f32_e32 v58, v58
	v_exp_f32_e32 v43, v43
	v_exp_f32_e32 v59, v59
	v_exp_f32_e32 v44, v44
	v_exp_f32_e32 v60, v60
	v_exp_f32_e32 v45, v45
	v_exp_f32_e32 v61, v61
	v_exp_f32_e32 v46, v46
	v_exp_f32_e32 v62, v62
	v_exp_f32_e32 v47, v47
	v_exp_f32_e32 v63, v63
	v_exp_f32_e32 v48, v48
	v_exp_f32_e32 v64, v64
	v_exp_f32_e32 v49, v49
	v_exp_f32_e32 v65, v65
	v_add_f32_e32 v138, 1.0, v37
	v_add_f32_e32 v139, 1.0, v41
	v_add_f32_e32 v140, 1.0, v45
	v_add_f32_e32 v141, 1.0, v49
	v_add_f32_e32 v142, 1.0, v53
	v_add_f32_e32 v143, 1.0, v57
	v_add_f32_e32 v144, 1.0, v61
	v_add_f32_e32 v145, 1.0, v65
	v_fma_f32 v138, v36, v138, v138
	v_fma_f32 v139, v40, v139, v139
	v_fma_f32 v140, v44, v140, v140
	v_fma_f32 v141, v48, v141, v141
	v_fma_f32 v142, v52, v142, v142
	v_fma_f32 v143, v56, v143, v143
	v_fma_f32 v144, v60, v144, v144
	v_fma_f32 v145, v64, v145, v145
	v_fma_f32 v138, v35, v138, v138
	v_fma_f32 v139, v39, v139, v139
	v_fma_f32 v140, v43, v140, v140
	v_fma_f32 v141, v47, v141, v141
	v_fma_f32 v142, v51, v142, v142
	v_fma_f32 v143, v55, v143, v143
	v_fma_f32 v144, v59, v144, v144
	v_fma_f32 v145, v63, v145, v145
	v_fma_f32 v138, v34, v138, v138
	v_fma_f32 v139, v38, v139, v139
	v_fma_f32 v140, v42, v140, v140
	v_fma_f32 v141, v46, v141, v141
	v_fma_f32 v142, v50, v142, v142
	v_fma_f32 v143, v54, v143, v143
	v_fma_f32 v144, v58, v144, v144
	v_fma_f32 v145, v62, v145, v145
	v_max3_f32 v127, v138, v139, v140
	v_max3_f32 v128, v141, v142, v143
	v_max3_f32 v127, v127, v144, v145
	v_max_f32_e32 v127, v127, v128
	v_cmp_lt_f32_e32 vcc, 0x6f800000, v127
	s_cbranch_vccnz .Lsbq_slow
; __device__ __forceinline__ float vmul(float a, float b) { float r; asm("v_mul_f32 %0, %1, %2" : "=v"(r) : "v"(a), "v"(b)); return r; }
; __device__ __forceinline__ float vsub(float a, float b) { float r; asm("v_sub_f32 %0, %1, %2" : "=v"(r) : "v"(a), "v"(b)); return r; }
; __device__ __forceinline__ float swap32(float x) { auto rr = __builtin_amdgcn_permlane32_swap(__float_as_uint(x), __float_as_uint(x), false, false); return __uint_as_float(((unsigned)(threadIdx.x & 32)) ? rr[0] : rr[1]); }
; __device__ __forceinline__ float swap_sel(float a, float b) { auto rr = __builtin_amdgcn_permlane32_swap(__float_as_uint(a), __float_as_uint(b), false, false); return __uint_as_float(((unsigned)(threadIdx.x & 32)) ? rr[0] : rr[1]); }
; #define V_WAIT(vf) asm volatile("s_waitcnt lgkmcnt(0)" : "+v"(vf[0]), "+v"(vf[1]), "+v"(vf[2]), "+v"(vf[3]), "+v"(vf[4]), "+v"(vf[5]), "+v"(vf[6]), "+v"(vf[7]))
; template <bool DIAG> __device__ __forceinline__ void sb_tile(const LAS unsigned char* ks, int vpo, const bf16x8 (&qr)[4], f32x16& o0, f32x16& o1, float& carry, int kb, int q, int r32, int hi) {
;     ...
;     float I[9]; I[8] = 1.f; I[7] = s1[12];
; #pragma unroll
;     for (int g = 6; g >= 0; --g) I[g] = vmul(I[g + 1], g < 4 ? s0[4 * g] : s1[4 * (g - 4)]);
;     float off[8];
; #pragma unroll
;     for (int g = 0; g < 8; ++g) {
;         const float x = swap_sel(I[g], I[g + 1]);
;         off[g] = (g == 7) ? vmul(carry, x) : vmul(vmul(carry, I[g + 1]), x);
;     }
;     carry = vmul(carry, vmul(I[0], swap32(I[0])));
;     f32x16 w0, w1;
; #pragma unroll
;     for (int g = 0; g < 4; ++g) {
;         { const float o = off[g]; const float S3 = vmul(s0[4 * g + 3], o), S2 = vmul(s0[4 * g + 2], o), S1 = vmul(s0[4 * g + 1], o), S0 = vmul(s0[4 * g], o);
;           w0[4 * g + 3] = vsub(o, S3); w0[4 * g + 2] = vsub(S3, S2); w0[4 * g + 1] = vsub(S2, S1); w0[4 * g] = vsub(S1, S0); }
;         { const float o = off[4 + g]; const float S3 = vmul(s1[4 * g + 3], o), S2 = vmul(s1[4 * g + 2], o), S1 = vmul(s1[4 * g + 1], o), S0 = vmul(s1[4 * g], o);
;           w1[4 * g + 3] = vsub(o, S3); w1[4 * g + 2] = vsub(S3, S2); w1[4 * g + 1] = vsub(S2, S1); w1[4 * g] = vsub(S1, S0); }
;     }
;     V_WAIT(vf);
;     pv_tile(o0, o1, vf, w0, w1);
	v_rcp_f32_e32 v145, v145
	v_rcp_f32_e32 v144, v144
	v_rcp_f32_e32 v143, v143
	v_rcp_f32_e32 v142, v142
	v_rcp_f32_e32 v141, v141
	v_rcp_f32_e32 v140, v140
	v_rcp_f32_e32 v139, v139
	v_rcp_f32_e32 v138, v138
	v_mov_b32_e32 v136, 1.0
	v_mul_f32_e32 v127, v145, v144
	v_mul_f32_e32 v128, v127, v143
	v_mul_f32_e32 v129, v128, v142
	v_mul_f32_e32 v130, v129, v141
	v_mul_f32_e32 v131, v130, v140
	v_mul_f32_e32 v132, v131, v139
	v_mul_f32_e32 v133, v132, v138
	v_mov_b32_e32 v134, v132
	v_mov_b32_e32 v135, v133
	v_mov_b32_e32 v137, v133
	s_nop 0
	v_permlane32_swap_b32_e32 v135, v134
	v_cndmask_b32_e64 v134, v135, v134, s[4:5]
	v_mul_f32_e32 v135, v125, v132
	v_mul_f32_e32 v134, v135, v134
	v_mov_b32_e32 v135, v131
	v_mul_f32_e32 v138, v138, v134
	v_mul_f32_e32 v34, v34, v138
	v_permlane32_swap_b32_e32 v132, v135
	v_cndmask_b32_e64 v132, v132, v135, s[4:5]
	v_mul_f32_e32 v135, v125, v131
	v_mul_f32_e32 v132, v135, v132
	v_add_f32_e32 v138, v138, v34
	v_mul_f32_e32 v35, v35, v138
	v_add_f32_e32 v138, v138, v35
	v_mul_f32_e32 v36, v36, v138
	v_add_f32_e32 v138, v138, v36
	v_mul_f32_e32 v37, v37, v138
	v_mov_b32_e32 v135, v130
	v_mul_f32_e32 v139, v139, v132
	v_mul_f32_e32 v38, v38, v139
	v_permlane32_swap_b32_e32 v131, v135
	v_cndmask_b32_e64 v131, v131, v135, s[4:5]
	v_mul_f32_e32 v135, v125, v130
	v_mul_f32_e32 v131, v135, v131
	v_add_f32_e32 v139, v139, v38
	v_mul_f32_e32 v39, v39, v139
	v_add_f32_e32 v139, v139, v39
	v_mul_f32_e32 v40, v40, v139
	v_add_f32_e32 v139, v139, v40
	v_mul_f32_e32 v41, v41, v139
	v_mov_b32_e32 v135, v129
	v_mul_f32_e32 v140, v140, v131
	v_mul_f32_e32 v42, v42, v140
	v_permlane32_swap_b32_e32 v130, v135
	v_cndmask_b32_e64 v130, v130, v135, s[4:5]
	v_mul_f32_e32 v135, v125, v129
	v_mul_f32_e32 v130, v135, v130
	v_add_f32_e32 v140, v140, v42
	v_mul_f32_e32 v43, v43, v140
	v_add_f32_e32 v140, v140, v43
	v_mul_f32_e32 v44, v44, v140
	v_add_f32_e32 v140, v140, v44
	v_mul_f32_e32 v45, v45, v140
	v_mov_b32_e32 v135, v128
	v_mul_f32_e32 v141, v141, v130
	v_mul_f32_e32 v46, v46, v141
	v_permlane32_swap_b32_e32 v129, v135
	v_cndmask_b32_e64 v129, v129, v135, s[4:5]
	v_mul_f32_e32 v135, v125, v128
	v_mul_f32_e32 v129, v135, v129
	v_add_f32_e32 v141, v141, v46
	v_mul_f32_e32 v47, v47, v141
	v_add_f32_e32 v141, v141, v47
	v_mul_f32_e32 v48, v48, v141
	v_add_f32_e32 v141, v141, v48
	v_mul_f32_e32 v49, v49, v141
	v_mov_b32_e32 v135, v127
	v_mul_f32_e32 v142, v142, v129
	v_mul_f32_e32 v50, v50, v142
	v_permlane32_swap_b32_e32 v128, v135
	v_cndmask_b32_e64 v128, v128, v135, s[4:5]
	v_mul_f32_e32 v135, v125, v127
	v_mul_f32_e32 v128, v135, v128
	v_add_f32_e32 v142, v142, v50
	v_mul_f32_e32 v51, v51, v142
	v_add_f32_e32 v142, v142, v51
	v_mul_f32_e32 v52, v52, v142
	v_add_f32_e32 v142, v142, v52
	v_mul_f32_e32 v53, v53, v142
	v_mov_b32_e32 v135, v145
	v_mul_f32_e32 v143, v143, v128
	v_mul_f32_e32 v54, v54, v143
	v_permlane32_swap_b32_e32 v127, v135
	v_cndmask_b32_e64 v127, v127, v135, s[4:5]
	v_mul_f32_e32 v135, v125, v145
	v_mul_f32_e32 v135, v135, v127
	v_add_f32_e32 v143, v143, v54
	v_mul_f32_e32 v55, v55, v143
	v_add_f32_e32 v143, v143, v55
	v_mul_f32_e32 v56, v56, v143
	v_add_f32_e32 v143, v143, v56
	v_mul_f32_e32 v57, v57, v143
	v_mov_b32_e32 v127, v145
	v_mul_f32_e32 v144, v144, v135
	v_mul_f32_e32 v58, v58, v144
	v_permlane32_swap_b32_e32 v127, v136
	v_cndmask_b32_e64 v127, v127, v136, s[4:5]
	v_mul_f32_e32 v136, v125, v127
	v_add_f32_e32 v144, v144, v58
	v_mul_f32_e32 v59, v59, v144
	v_add_f32_e32 v144, v144, v59
	v_mul_f32_e32 v60, v60, v144
	v_add_f32_e32 v144, v144, v60
	v_mul_f32_e32 v61, v61, v144
	v_mov_b32_e32 v127, v133
	v_mul_f32_e32 v145, v145, v136
	v_mul_f32_e32 v62, v62, v145
	v_permlane32_swap_b32_e32 v127, v137
	v_cndmask_b32_e64 v127, v127, v137, s[4:5]
	v_mul_f32_e32 v127, v133, v127
	v_add_f32_e32 v145, v145, v62
	v_mul_f32_e32 v63, v63, v145
	v_add_f32_e32 v145, v145, v63
	v_mul_f32_e32 v64, v64, v145
	v_add_f32_e32 v145, v145, v64
	v_mul_f32_e32 v65, v65, v145
	v_mul_f32_e32 v125, v125, v127
	s_waitcnt lgkmcnt(0)
	v_cvt_pk_bf16_f32 v128, v34, v35
	v_cvt_pk_bf16_f32 v129, v36, v37
	v_cvt_pk_bf16_f32 v130, v38, v39
	v_cvt_pk_bf16_f32 v131, v40, v41
	s_nop 1
	v_mfma_f32_32x32x16_bf16 v[18:33], v[110:113], v[128:131], v[18:33]
	v_mfma_f32_32x32x16_bf16 v[2:17], v[106:109], v[128:131], v[2:17]
	v_cvt_pk_bf16_f32 v106, v42, v43
	v_cvt_pk_bf16_f32 v107, v44, v45
	v_cvt_pk_bf16_f32 v108, v46, v47
	v_cvt_pk_bf16_f32 v109, v48, v49
	s_nop 1
	v_mfma_f32_32x32x16_bf16 v[18:33], v[102:105], v[106:109], v[18:33]
	v_mfma_f32_32x32x16_bf16 v[2:17], v[98:101], v[106:109], v[2:17]
	v_cvt_pk_bf16_f32 v98, v50, v51
	v_cvt_pk_bf16_f32 v99, v52, v53
	v_cvt_pk_bf16_f32 v100, v54, v55
	v_cvt_pk_bf16_f32 v101, v56, v57
	s_nop 1
	v_mfma_f32_32x32x16_bf16 v[18:33], v[94:97], v[98:101], v[18:33]
	v_mfma_f32_32x32x16_bf16 v[2:17], v[90:93], v[98:101], v[2:17]
	v_cvt_pk_bf16_f32 v90, v58, v59
	v_cvt_pk_bf16_f32 v91, v60, v61
	v_cvt_pk_bf16_f32 v92, v62, v63
	v_cvt_pk_bf16_f32 v93, v64, v65
	s_nop 1
	v_mfma_f32_32x32x16_bf16 v[18:33], v[86:89], v[90:93], v[18:33]
	v_mfma_f32_32x32x16_bf16 v[2:17], v[82:85], v[90:93], v[2:17]
	s_branch .LBB0_887
; __device__ __forceinline__ float fexp2(float x) { return __builtin_amdgcn_exp2f(x); }
; __device__ __forceinline__ float frcp(float x) { return __builtin_amdgcn_rcpf(x); }
; __device__ __forceinline__ float vmul(float a, float b) { float r; asm("v_mul_f32 %0, %1, %2" : "=v"(r) : "v"(a), "v"(b)); return r; }
; template <bool DIAG> __device__ __forceinline__ void sb_tile(const LAS unsigned char* ks, int vpo, const bf16x8 (&qr)[4], f32x16& o0, f32x16& o1, float& carry, int kb, int q, int r32, int hi) {
;     ...
;     for (int r = 0; r < 16; ++r) { s0[r] = frcp(1.f + fexp2(z0[r])); s1[r] = frcp(1.f + fexp2(z1[r])); }
;     ...
;     for (int g = 0; g < 4; ++g) {
;         s0[4 * g + 2] = vmul(s0[4 * g + 2], s0[4 * g + 3]); s0[4 * g + 1] = vmul(s0[4 * g + 1], s0[4 * g + 2]); s0[4 * g] = vmul(s0[4 * g], s0[4 * g + 1]);
;         s1[4 * g + 2] = vmul(s1[4 * g + 2], s1[4 * g + 3]); s1[4 * g + 1] = vmul(s1[4 * g + 1], s1[4 * g + 2]); s1[4 * g] = vmul(s1[4 * g], s1[4 * g + 1]);
.Lsbq_slow:
	v_add_f32_e32 v34, 1.0, v34
	v_add_f32_e32 v50, 1.0, v50
	v_add_f32_e32 v35, 1.0, v35
	v_add_f32_e32 v51, 1.0, v51
	v_add_f32_e32 v36, 1.0, v36
	v_add_f32_e32 v52, 1.0, v52
	v_add_f32_e32 v37, 1.0, v37
	v_add_f32_e32 v53, 1.0, v53
	v_add_f32_e32 v38, 1.0, v38
	v_add_f32_e32 v54, 1.0, v54
	v_add_f32_e32 v39, 1.0, v39
	v_add_f32_e32 v55, 1.0, v55
	v_add_f32_e32 v40, 1.0, v40
	v_add_f32_e32 v56, 1.0, v56
	v_add_f32_e32 v41, 1.0, v41
	v_add_f32_e32 v57, 1.0, v57
	v_add_f32_e32 v42, 1.0, v42
	v_add_f32_e32 v58, 1.0, v58
	v_add_f32_e32 v43, 1.0, v43
	v_add_f32_e32 v59, 1.0, v59
	v_add_f32_e32 v44, 1.0, v44
	v_add_f32_e32 v60, 1.0, v60
	v_add_f32_e32 v45, 1.0, v45
	v_add_f32_e32 v61, 1.0, v61
	v_add_f32_e32 v46, 1.0, v46
	v_add_f32_e32 v62, 1.0, v62
	v_add_f32_e32 v47, 1.0, v47
	v_add_f32_e32 v63, 1.0, v63
	v_add_f32_e32 v48, 1.0, v48
	v_add_f32_e32 v64, 1.0, v64
	v_add_f32_e32 v49, 1.0, v49
	v_add_f32_e32 v65, 1.0, v65
	v_rcp_f32_e32 v34, v34
	v_rcp_f32_e32 v50, v50
	v_rcp_f32_e32 v35, v35
	v_rcp_f32_e32 v51, v51
	v_rcp_f32_e32 v36, v36
	v_rcp_f32_e32 v52, v52
	v_rcp_f32_e32 v37, v37
	v_rcp_f32_e32 v53, v53
	v_rcp_f32_e32 v38, v38
	v_rcp_f32_e32 v54, v54
	v_rcp_f32_e32 v39, v39
	v_rcp_f32_e32 v55, v55
	v_rcp_f32_e32 v40, v40
	v_rcp_f32_e32 v56, v56
	v_rcp_f32_e32 v41, v41
	v_rcp_f32_e32 v57, v57
	v_rcp_f32_e32 v42, v42
	v_rcp_f32_e32 v58, v58
	v_rcp_f32_e32 v43, v43
	v_rcp_f32_e32 v59, v59
	v_rcp_f32_e32 v44, v44
	v_rcp_f32_e32 v60, v60
	v_rcp_f32_e32 v45, v45
	v_rcp_f32_e32 v61, v61
	v_rcp_f32_e32 v46, v46
	v_rcp_f32_e32 v62, v62
	v_rcp_f32_e32 v47, v47
	v_rcp_f32_e32 v63, v63
	v_rcp_f32_e32 v48, v48
	v_rcp_f32_e32 v64, v64
	v_rcp_f32_e32 v49, v49
	v_rcp_f32_e32 v65, v65
	s_nop 0
	v_mov_b32_e32 v136, 1.0
	v_mul_f32 v36, v36, v37
	v_mul_f32 v52, v52, v53
	v_mul_f32 v40, v40, v41
	v_mul_f32 v56, v56, v57
	v_mul_f32 v44, v44, v45
	v_mul_f32 v60, v60, v61
	s_nop 0
	v_mul_f32 v35, v35, v36
	v_mul_f32 v51, v51, v52
	v_mul_f32 v39, v39, v40
	v_mul_f32 v55, v55, v56
	v_mul_f32 v43, v43, v44
	v_mul_f32 v59, v59, v60
	s_nop 0
	v_mul_f32 v34, v34, v35
	v_mul_f32 v50, v50, v51
	v_mul_f32 v38, v38, v39
	v_mul_f32 v54, v54, v55
	v_mul_f32 v42, v42, v43
	v_mul_f32 v58, v58, v59
	v_mul_f32 v48, v48, v49
	v_mul_f32 v64, v64, v65
	s_waitcnt lgkmcnt(0)
; __device__ __forceinline__ float vmul(float a, float b) { float r; asm("v_mul_f32 %0, %1, %2" : "=v"(r) : "v"(a), "v"(b)); return r; }
; __device__ __forceinline__ float vsub(float a, float b) { float r; asm("v_sub_f32 %0, %1, %2" : "=v"(r) : "v"(a), "v"(b)); return r; }
; __device__ __forceinline__ float swap32(float x) { auto rr = __builtin_amdgcn_permlane32_swap(__float_as_uint(x), __float_as_uint(x), false, false); return __uint_as_float(((unsigned)(threadIdx.x & 32)) ? rr[0] : rr[1]); }
; #define V_WAIT(vf) asm volatile("s_waitcnt lgkmcnt(0)" : "+v"(vf[0]), "+v"(vf[1]), "+v"(vf[2]), "+v"(vf[3]), "+v"(vf[4]), "+v"(vf[5]), "+v"(vf[6]), "+v"(vf[7]))
; template <bool DIAG> __device__ __forceinline__ void sb_tile(const LAS unsigned char* ks, int vpo, const bf16x8 (&qr)[4], f32x16& o0, f32x16& o1, float& carry, int kb, int q, int r32, int hi) {
;     ...
;     for (int g = 0; g < 4; ++g) {
;         s0[4 * g + 2] = vmul(s0[4 * g + 2], s0[4 * g + 3]); s0[4 * g + 1] = vmul(s0[4 * g + 1], s0[4 * g + 2]); s0[4 * g] = vmul(s0[4 * g], s0[4 * g + 1]);
;         s1[4 * g + 2] = vmul(s1[4 * g + 2], s1[4 * g + 3]); s1[4 * g + 1] = vmul(s1[4 * g + 1], s1[4 * g + 2]); s1[4 * g] = vmul(s1[4 * g], s1[4 * g + 1]);
;     }
;     float I[9]; I[8] = 1.f; I[7] = s1[12];
; #pragma unroll
;     for (int g = 6; g >= 0; --g) I[g] = vmul(I[g + 1], g < 4 ? s0[4 * g] : s1[4 * (g - 4)]);
;     float off[8];
; #pragma unroll
;     for (int g = 0; g < 8; ++g) {
;         const float x = swap_sel(I[g], I[g + 1]);
;         off[g] = (g == 7) ? vmul(carry, x) : vmul(vmul(carry, I[g + 1]), x);
;     }
;     carry = vmul(carry, vmul(I[0], swap32(I[0])));
;     f32x16 w0, w1;
; #pragma unroll
;     for (int g = 0; g < 4; ++g) {
;         { const float o = off[g]; const float S3 = vmul(s0[4 * g + 3], o), S2 = vmul(s0[4 * g + 2], o), S1 = vmul(s0[4 * g + 1], o), S0 = vmul(s0[4 * g], o);
;           w0[4 * g + 3] = vsub(o, S3); w0[4 * g + 2] = vsub(S3, S2); w0[4 * g + 1] = vsub(S2, S1); w0[4 * g] = vsub(S1, S0); }
;         { const float o = off[4 + g]; const float S3 = vmul(s1[4 * g + 3], o), S2 = vmul(s1[4 * g + 2], o), S1 = vmul(s1[4 * g + 1], o), S0 = vmul(s1[4 * g], o);
;           w1[4 * g + 3] = vsub(o, S3); w1[4 * g + 2] = vsub(S3, S2); w1[4 * g + 1] = vsub(S2, S1); w1[4 * g] = vsub(S1, S0); }
;     }
;     V_WAIT(vf);
;     pv_tile(o0, o1, vf, w0, w1);
	s_mov_b64 s[10:11], 0
	v_mul_f32 v47, v47, v48
	v_mul_f32 v63, v63, v64
	s_nop 0
	v_mul_f32 v46, v46, v47
	v_mul_f32 v62, v62, v63
	s_nop 0
	v_mul_f32 v127, v62, v58
	s_nop 0
	v_mul_f32 v128, v127, v54
	s_nop 0
	v_mul_f32 v129, v128, v50
	s_nop 0
	v_mul_f32 v130, v129, v46
	s_nop 0
	v_mul_f32 v131, v130, v42
	s_nop 0
	v_mul_f32 v132, v131, v38
	s_nop 0
	v_mul_f32 v133, v132, v34
	v_mov_b32_e32 v134, v132
	v_mov_b32_e32 v135, v133
	s_nop 1
	v_permlane32_swap_b32_e32 v135, v134
	v_cndmask_b32_e64 v134, v135, v134, s[4:5]
	v_mul_f32 v135, v125, v132
	v_mov_b32_e32 v137, v133
	v_mul_f32 v134, v135, v134
	v_mov_b32_e32 v135, v131
	s_nop 1
	v_permlane32_swap_b32_e32 v132, v135
	v_cndmask_b32_e64 v132, v132, v135, s[4:5]
	v_mul_f32 v135, v125, v131
	v_mul_f32 v37, v37, v134
	v_mul_f32 v36, v36, v134
	v_mul_f32 v35, v35, v134
	v_mul_f32 v34, v34, v134
	s_nop 0
	v_mul_f32 v132, v135, v132
	v_mov_b32_e32 v135, v130
	s_nop 1
	v_permlane32_swap_b32_e32 v131, v135
	v_cndmask_b32_e64 v131, v131, v135, s[4:5]
	v_mul_f32 v135, v125, v130
	v_sub_f32 v34, v35, v34
	v_mul_f32 v40, v40, v132
	v_mul_f32 v39, v39, v132
	v_mul_f32 v38, v38, v132
	s_nop 0
	v_mul_f32 v131, v135, v131
	v_mov_b32_e32 v135, v129
	s_nop 1
	v_permlane32_swap_b32_e32 v130, v135
	v_cndmask_b32_e64 v130, v130, v135, s[4:5]
	v_mul_f32 v135, v125, v129
	v_sub_f32 v38, v39, v38
	v_mul_f32 v44, v44, v131
	v_mul_f32 v43, v43, v131
	v_mul_f32 v42, v42, v131
	s_nop 0
	v_mul_f32 v130, v135, v130
	v_mov_b32_e32 v135, v128
	s_nop 1
	v_permlane32_swap_b32_e32 v129, v135
	v_cndmask_b32_e64 v129, v129, v135, s[4:5]
	v_mul_f32 v135, v125, v128
	v_sub_f32 v145, v44, v43
	v_sub_f32 v146, v43, v42
	s_nop 0
	v_mul_f32 v129, v135, v129
	v_mov_b32_e32 v135, v127
	s_nop 1
	v_permlane32_swap_b32_e32 v128, v135
	v_cndmask_b32_e64 v128, v128, v135, s[4:5]
	v_mul_f32 v135, v125, v127
	v_mul_f32 v52, v52, v129
	v_mul_f32 v50, v50, v129
	v_mul_f32 v51, v51, v129
	s_nop 0
	v_mul_f32 v128, v135, v128
	v_mov_b32_e32 v135, v62
	s_nop 1
	v_permlane32_swap_b32_e32 v127, v135
	v_cndmask_b32_e64 v127, v127, v135, s[4:5]
	v_mul_f32 v135, v125, v62
	v_sub_f32 v139, v51, v50
	v_mul_f32 v50, v56, v128
	v_sub_f32 v138, v52, v51
	v_mul_f32 v51, v55, v128
	s_nop 0
	v_mul_f32 v135, v135, v127
	v_mov_b32_e32 v127, v62
	s_nop 1
	v_permlane32_swap_b32_e32 v127, v136
	v_cndmask_b32_e64 v127, v127, v136, s[4:5]
	v_mul_f32 v136, v125, v127
	v_mov_b32_e32 v127, v133
	s_nop 1
	v_permlane32_swap_b32_e32 v127, v137
	v_cndmask_b32_e64 v127, v127, v137, s[4:5]
	v_mul_f32 v127, v133, v127
	v_sub_f32 v133, v134, v37
	v_sub_f32 v37, v37, v36
	v_sub_f32 v36, v36, v35
	v_mul_f32 v35, v53, v129
	v_mul_f32 v42, v60, v135
	v_mul_f32 v43, v59, v135
	v_sub_f32 v141, v50, v51
	s_nop 0
	v_mul_f32 v127, v125, v127
	v_sub_f32 v134, v129, v35
	v_sub_f32 v137, v35, v52
	v_mul_f32 v35, v41, v132
	v_sub_f32 v148, v42, v43
	v_mul_f32 v52, v54, v128
	v_cvt_pk_bf16_f32 v129, v37, v133
	v_sub_f32 v41, v132, v35
	v_sub_f32 v35, v35, v40
	v_sub_f32 v40, v40, v39
	v_mul_f32 v39, v57, v128
	v_sub_f32 v142, v51, v52
	s_nop 0
	v_sub_f32 v132, v128, v39
	v_sub_f32 v140, v39, v50
	v_mul_f32 v39, v45, v131
	v_cvt_pk_bf16_f32 v128, v34, v36
	v_sub_f32 v143, v131, v39
	v_sub_f32 v144, v39, v44
	v_mul_f32 v39, v61, v135
	v_mul_f32 v44, v58, v135
	v_cvt_pk_bf16_f32 v131, v35, v41
	v_sub_f32 v135, v135, v39
	v_sub_f32 v147, v39, v42
	v_sub_f32 v149, v43, v44
	v_mul_f32 v39, v49, v130
	v_mul_f32 v42, v48, v130
	v_mul_f32 v43, v47, v130
	v_mul_f32 v44, v46, v130
	s_nop 0
	v_sub_f32 v150, v130, v39
	v_sub_f32 v151, v39, v42
	v_sub_f32 v152, v42, v43
	v_sub_f32 v153, v43, v44
	v_mul_f32 v39, v65, v136
	v_mul_f32 v42, v64, v136
	v_mul_f32 v43, v63, v136
	v_mul_f32 v44, v62, v136
	v_cvt_pk_bf16_f32 v130, v38, v40
	v_sub_f32 v136, v136, v39
	v_sub_f32 v154, v39, v42
	v_sub_f32 v155, v42, v43
	v_sub_f32 v156, v43, v44
	s_nop 1
	v_mfma_f32_32x32x16_bf16 v[18:33], v[110:113], v[128:131], v[18:33]
	v_mfma_f32_32x32x16_bf16 v[2:17], v[106:109], v[128:131], v[2:17]
	v_cvt_pk_bf16_f32 v106, v146, v145
	v_cvt_pk_bf16_f32 v107, v144, v143
	v_cvt_pk_bf16_f32 v108, v153, v152
	v_cvt_pk_bf16_f32 v109, v151, v150
	s_nop 1
	v_mfma_f32_32x32x16_bf16 v[18:33], v[102:105], v[106:109], v[18:33]
	v_mfma_f32_32x32x16_bf16 v[2:17], v[98:101], v[106:109], v[2:17]
	v_cvt_pk_bf16_f32 v98, v139, v138
	v_cvt_pk_bf16_f32 v99, v137, v134
	v_cvt_pk_bf16_f32 v100, v142, v141
	v_cvt_pk_bf16_f32 v101, v140, v132
	s_nop 1
	v_mfma_f32_32x32x16_bf16 v[18:33], v[94:97], v[98:101], v[18:33]
	v_mfma_f32_32x32x16_bf16 v[2:17], v[90:93], v[98:101], v[2:17]
	v_cvt_pk_bf16_f32 v90, v149, v148
	v_cvt_pk_bf16_f32 v91, v147, v135
	v_cvt_pk_bf16_f32 v92, v156, v155
	v_cvt_pk_bf16_f32 v93, v154, v136
	s_nop 1
	v_mfma_f32_32x32x16_bf16 v[18:33], v[86:89], v[90:93], v[18:33]
	v_mfma_f32_32x32x16_bf16 v[2:17], v[82:85], v[90:93], v[2:17]
	v_mov_b32_e32 v125, v127
	s_branch .LBB0_887
